# init_x row loop: all 12 loads of a row issued together with counted waits instead of 6 serial round trips
# baseline (speedup 1.0000x reference)
; __device__ __forceinline__ unsigned cvt_pk_bf16(float lo, float hi) { unsigned r; asm volatile("v_cvt_pk_bf16_f32 %0, %1, %2" : "=v"(r) : "v"(lo), "v"(hi)); return r; }
; __device__ __forceinline__ void ph_init_x(const Frame& F) {
;     ...
;     for (int row = gw; row < TT; row += nw) {
;         const float* src = row < TC ? ctx + (size_t)row * DM : x + (size_t)(row - TC) * DM;
;         const float* m = F.mods + (size_t)(0 * 5 + slot_of_row(row)) * 6144;
; #pragma unroll
;         for (int hh = 0; hh < 2; ++hh) { const int k = hh * 512 + F.lane * 8;
;             const f32x4 v0 = *(const f32x4*)(src + k), v1 = *(const f32x4*)(src + k + 4);
;             *(f32x4*)(F.X + (size_t)row * DM + k) = v0; *(f32x4*)(F.X + (size_t)row * DM + k + 4) = v1;
;             const f32x4 s0 = *(const f32x4*)(m + 1024 + k), s1 = *(const f32x4*)(m + 1024 + k + 4), b0 = *(const f32x4*)(m + k), b1 = *(const f32x4*)(m + k + 4);
;             const f32x4 h0 = v0 * (s0 + 1.0f) + b0, h1 = v1 * (s1 + 1.0f) + b1;
;             u32x4 w; w.x = cvt_pk_bf16(h0[0], h0[1]); w.y = cvt_pk_bf16(h0[2], h0[3]); w.z = cvt_pk_bf16(h1[0], h1[1]); w.w = cvt_pk_bf16(h1[2], h1[3]);
;             *(u32x4*)(F.HB + (size_t)row * DM + k) = w; }
;     }
.LBB0_83:
	v_lshl_add_u64 v[32:33], s[16:17], 0, v[6:7]
	global_load_dwordx4 v[8:11], v[32:33], off
	global_load_dwordx4 v[12:15], v[32:33], off offset:16
	global_load_dwordx4 v[42:45], v[32:33], off offset:2048
	global_load_dwordx4 v[46:49], v[32:33], off offset:2064
	s_lshr_b32 s6, s6, 13
	s_and_b64 s[14:15], s[14:15], exec
	s_cselect_b32 s6, 4, s6
	s_mul_hi_u32 s15, s6, 0x6000
	s_mulk_i32 s6, 0x6000
	s_add_u32 s14, s28, s6
	s_addc_u32 s15, s29, s15
	s_lshl_b64 s[16:17], s[12:13], 12
	v_lshl_add_u64 v[36:37], s[14:15], 0, v[6:7]
	v_lshl_add_u64 v[34:35], v[2:3], 0, s[16:17]
	v_lshl_add_u64 v[38:39], v[36:37], 0, s[8:9]
	s_lshl_b64 s[12:13], s[12:13], 11
	v_lshl_add_u64 v[40:41], v[4:5], 0, s[12:13]
	s_add_u32 s10, s10, s80
	s_addc_u32 s11, s11, s81
	s_add_u32 s0, s0, s4
	s_addc_u32 s1, s1, s5
	s_cmp_lt_i32 s10, 0x8400
	global_load_dwordx4 v[16:19], v[38:39], off
	global_load_dwordx4 v[20:23], v[38:39], off offset:16
	global_load_dwordx4 v[24:27], v[36:37], off
	global_load_dwordx4 v[28:31], v[36:37], off offset:16
	global_load_dwordx4 v[50:53], v[38:39], off offset:2048
	global_load_dwordx4 v[54:57], v[38:39], off offset:2064
	global_load_dwordx4 v[58:61], v[36:37], off offset:2048
	global_load_dwordx4 v[62:65], v[36:37], off offset:2064
	s_waitcnt vmcnt(8)
	global_store_dwordx4 v[34:35], v[8:11], off
	global_store_dwordx4 v[34:35], v[12:15], off offset:16
	global_store_dwordx4 v[34:35], v[42:45], off offset:2048
	global_store_dwordx4 v[34:35], v[46:49], off offset:2064
	s_waitcnt vmcnt(4)
	v_pk_add_f32 v[18:19], v[18:19], 1.0 op_sel_hi:[1,0]
	v_pk_add_f32 v[16:17], v[16:17], 1.0 op_sel_hi:[1,0]
	v_pk_add_f32 v[22:23], v[22:23], 1.0 op_sel_hi:[1,0]
	v_pk_add_f32 v[20:21], v[20:21], 1.0 op_sel_hi:[1,0]
	v_pk_add_f32 v[52:53], v[52:53], 1.0 op_sel_hi:[1,0]
	v_pk_add_f32 v[50:51], v[50:51], 1.0 op_sel_hi:[1,0]
	v_pk_add_f32 v[56:57], v[56:57], 1.0 op_sel_hi:[1,0]
	v_pk_add_f32 v[54:55], v[54:55], 1.0 op_sel_hi:[1,0]
	v_pk_fma_f32 v[10:11], v[10:11], v[18:19], v[26:27]
	v_pk_fma_f32 v[8:9], v[8:9], v[16:17], v[24:25]
	v_pk_fma_f32 v[14:15], v[14:15], v[22:23], v[30:31]
	v_pk_fma_f32 v[12:13], v[12:13], v[20:21], v[28:29]
	v_pk_fma_f32 v[44:45], v[44:45], v[52:53], v[60:61]
	v_pk_fma_f32 v[42:43], v[42:43], v[50:51], v[58:59]
	v_pk_fma_f32 v[48:49], v[48:49], v[56:57], v[64:65]
	v_pk_fma_f32 v[46:47], v[46:47], v[54:55], v[62:63]
	v_cvt_pk_bf16_f32 v8, v8, v9
	v_cvt_pk_bf16_f32 v9, v10, v11
	s_nop 0
	v_cvt_pk_bf16_f32 v10, v12, v13
	v_cvt_pk_bf16_f32 v11, v14, v15
	global_store_dwordx4 v[40:41], v[8:11], off
	v_cvt_pk_bf16_f32 v42, v42, v43
	v_cvt_pk_bf16_f32 v43, v44, v45
	s_nop 0
	v_cvt_pk_bf16_f32 v44, v46, v47
	v_cvt_pk_bf16_f32 v45, v48, v49
	global_store_dwordx4 v[40:41], v[42:45], off offset:1024
	s_cbranch_scc0 .LBB0_88
